# speedup vs baseline: 1.0108x; 1.0108x over previous
.LBB0_41:
	s_or_b64 exec, exec, s[34:35]
	s_and_saveexec_b64 s[24:25], s[20:21]
	s_cbranch_execz .LBB0_43
	v_sub_u32_e32 v46, v46, v45
	v_add_u32_e32 v46, v46, v48
	ds_write_b32 v10, v46 offset:33568
	v_lshl_or_b32 v10, v45, 16, v46
	s_movk_i32 s3, 0xc8
	v_mov_b32_e32 v45, s2
	v_mad_u32_u24 v46, v0, s3, v45
	v_mov_b32_e32 v47, 0
	v_lshl_add_u64 v[46:47], v[46:47], 2, s[28:29]
	global_store_dword v[46:47], v10, off sc1

.LBB0_63:
	s_or_b64 exec, exec, s[2:3]
	v_lshrrev_b32_e32 v6, 2, v1
	v_lshrrev_b32_e32 v5, 4, v1
	v_and_b32_e32 v6, 8, v6
	s_mov_b32 s0, 0x1fffff0
	v_and_b32_e32 v4, 31, v1
	v_and_or_b32 v5, v5, s0, v6
	v_lshrrev_b32_e32 v1, 1, v1
	s_movk_i32 s0, 0x60
	v_and_or_b32 v1, v1, s0, v4
	v_lshl_or_b32 v4, v5, 7, v1
	v_ashrrev_i32_e32 v5, 31, v4
	v_lshl_add_u64 v[2:3], v[4:5], 2, v[2:3]
	global_load_dword v6, v[2:3], off offset:1024
	global_load_dword v7, v[2:3], off offset:1536
	global_load_dword v4, v[2:3], off offset:2048
	global_load_dword v5, v[2:3], off offset:3072
	global_load_dword v8, v[2:3], off offset:3584
	global_load_dword v9, v[2:3], off offset:2560
	global_load_dword v10, v[2:3], off
	global_load_dword v11, v[2:3], off offset:512
	v_ashrrev_i32_e32 v1, 31, v0
	v_lshl_add_u64 v[0:1], v[0:1], 4, s[4:5]
	s_waitcnt vmcnt(6)
	v_cvt_pk_f16_f32 v3, v6, v7
	s_waitcnt vmcnt(3)
	v_cvt_pk_f16_f32 v5, v5, v8
	s_waitcnt vmcnt(2)
	v_cvt_pk_f16_f32 v4, v4, v9
	s_waitcnt vmcnt(0)
	v_cvt_pk_f16_f32 v2, v10, v11
	global_store_dwordx4 v[0:1], v[2:5], off sc1
	s_endpgm

.LBB1_69:
	s_waitcnt lgkmcnt(0)
	v_cmp_gt_i32_e32 vcc, v4, v9
	s_nop 1
	v_cndmask_b32_e64 v10, v5, 0, vcc
	v_lshlrev_b32_e32 v12, 2, v10
	ds_read_b32 v12, v12 offset:34304
	v_or_b32_e32 v11, 0x80, v10
	s_waitcnt lgkmcnt(0)
	v_cmp_gt_i32_e32 vcc, v12, v9
	s_nop 1
	v_cndmask_b32_e32 v10, v11, v10, vcc
	v_lshlrev_b32_e32 v12, 2, v10
	ds_read_b32 v12, v12 offset:34048
	v_or_b32_e32 v11, 64, v10
	s_waitcnt lgkmcnt(0)
	v_cmp_gt_i32_e32 vcc, v12, v9
	s_nop 1
	v_cndmask_b32_e32 v10, v11, v10, vcc
	v_lshlrev_b32_e32 v12, 2, v10
	ds_read_b32 v12, v12 offset:33920
	v_or_b32_e32 v11, 32, v10
	s_waitcnt lgkmcnt(0)
	v_cmp_gt_i32_e32 vcc, v12, v9
	s_nop 1
	v_cndmask_b32_e32 v10, v11, v10, vcc
	v_lshlrev_b32_e32 v12, 2, v10
	ds_read_b32 v12, v12 offset:33856
	v_add_u32_e32 v11, 16, v10
	s_waitcnt lgkmcnt(0)
	v_cmp_gt_i32_e32 vcc, v12, v9
	s_nop 1
	v_cndmask_b32_e32 v10, v11, v10, vcc
	v_lshlrev_b32_e32 v12, 2, v10
	ds_read_b32 v12, v12 offset:33824
	v_add_u32_e32 v11, 8, v10
	s_waitcnt lgkmcnt(0)
	v_cmp_gt_i32_e32 vcc, v12, v9
	s_nop 1
	v_cndmask_b32_e32 v10, v11, v10, vcc
	v_lshlrev_b32_e32 v11, 2, v10
	ds_read_b32 v11, v11 offset:33808
	v_add_u32_e32 v12, 4, v10
	s_waitcnt lgkmcnt(0)
	v_cmp_gt_i32_e32 vcc, v11, v9
	s_nop 1
	v_cndmask_b32_e32 v10, v12, v10, vcc
	v_lshlrev_b32_e32 v11, 2, v10
	ds_read_b32 v11, v11 offset:33800
	v_add_u32_e32 v12, 2, v10
	s_waitcnt lgkmcnt(0)
	v_cmp_gt_i32_e32 vcc, v11, v9
	s_nop 1
	v_cndmask_b32_e32 v10, v12, v10, vcc
	v_lshlrev_b32_e32 v11, 2, v10
	ds_read_b32 v11, v11 offset:33796
	v_add_u32_e32 v12, 1, v10
	s_waitcnt lgkmcnt(0)
	v_cmp_gt_i32_e32 vcc, v11, v9
	s_nop 1
	v_cndmask_b32_e32 v10, v12, v10, vcc
	v_lshlrev_b32_e32 v10, 2, v10
	ds_read2st64_b32 v[10:11], v10 offset0:132 offset1:140
	s_waitcnt lgkmcnt(0)
	v_sub_u32_e32 v10, v11, v10
	v_add_u32_e32 v10, v9, v10
	v_ashrrev_i32_e32 v11, 31, v10
	v_lshl_add_u64 v[10:11], v[10:11], 3, s[52:53]
	global_load_dwordx2 v[10:11], v[10:11], off
	v_add_u32_e32 v9, 0x100, v9
	v_cmp_ge_i32_e32 vcc, v9, v26
	s_or_b64 s[18:19], vcc, s[18:19]
	s_waitcnt vmcnt(0)
	v_lshlrev_b32_sdwa v10, v8, sext(v10) dst_sel:DWORD dst_unused:UNUSED_PAD src0_sel:DWORD src1_sel:WORD_1
	ds_add_u32 v10, v7 offset:37168
	ds_add_f32 v10, v11 offset:38192
	s_andn2_b64 exec, exec, s[18:19]
	s_cbranch_execnz .LBB1_69
	s_or_b64 exec, exec, s[18:19]
	v_mov_b32_e32 v7, 0
	s_waitcnt lgkmcnt(0)
	s_barrier
	s_and_saveexec_b64 s[18:19], s[6:7]
	ds_read_b32 v7, v3 offset:37168
	s_or_b64 exec, exec, s[18:19]
	s_waitcnt lgkmcnt(0)
	ds_bpermute_b32 v4, v20, v7
	s_waitcnt lgkmcnt(0)
	v_cndmask_b32_e64 v4, v4, 0, s[50:51]
	v_add_u32_e32 v4, v4, v7
	ds_bpermute_b32 v5, v21, v4
	s_waitcnt lgkmcnt(0)
	v_cndmask_b32_e64 v5, v5, 0, s[4:5]
	v_add_u32_e32 v4, v5, v4
	ds_bpermute_b32 v5, v22, v4
	s_waitcnt lgkmcnt(0)
	v_cndmask_b32_e64 v5, v5, 0, s[8:9]
	v_add_u32_e32 v4, v5, v4
	ds_bpermute_b32 v5, v23, v4
	s_waitcnt lgkmcnt(0)
	v_cndmask_b32_e64 v5, v5, 0, s[10:11]
	v_add_u32_e32 v4, v5, v4
	ds_bpermute_b32 v5, v24, v4
	s_waitcnt lgkmcnt(0)
	v_cndmask_b32_e64 v5, v5, 0, s[12:13]
	v_add_u32_e32 v4, v5, v4
	ds_bpermute_b32 v5, v25, v4
	s_waitcnt lgkmcnt(0)
	v_cndmask_b32_e64 v5, v5, 0, s[14:15]
	v_add_u32_e32 v4, v5, v4
	s_and_saveexec_b64 s[18:19], s[16:17]
	v_lshlrev_b32_e32 v5, 2, v1
	ds_write_b32 v5, v4 offset:38720
	s_or_b64 exec, exec, s[18:19]
	s_waitcnt lgkmcnt(0)
	s_barrier
	s_and_saveexec_b64 s[20:21], s[6:7]
	s_cbranch_execz .LBB1_79
	v_mov_b32_e32 v5, 0
	ds_read_b32 v8, v5 offset:38720
	v_cmp_eq_u32_e32 vcc, 1, v1
	v_sub_u32_e32 v9, v4, v7
	v_lshl_or_b32 v4, s2, 7, v0
	s_mov_b32 s3, 0xc350
	s_waitcnt lgkmcnt(0)
	v_cndmask_b32_e32 v8, 0, v8, vcc
	v_add_u32_e32 v8, v8, v9
	v_cmp_gt_u32_e32 vcc, s3, v4
	ds_write_b32 v3, v8 offset:36640
	s_and_b64 exec, exec, vcc
	s_cbranch_execz .LBB1_79
	ds_read_b32 v13, v3 offset:38192
	v_add_u32_e32 v12, v8, v2
	v_lshlrev_b64 v[8:9], 2, v[4:5]
	v_lshl_add_u64 v[10:11], s[60:61], 0, v[8:9]
	v_add_u32_e32 v7, v12, v7
	v_lshl_add_u64 v[8:9], s[62:63], 0, v[8:9]
	global_store_dword v[8:9], v7, off sc1
	s_waitcnt lgkmcnt(0)
	v_add_f32_e32 v7, 1.0, v13
	v_cmp_lt_f32_e32 vcc, 0, v7
	v_mov_b32_e32 v8, v5
	global_store_dword v[10:11], v12, off sc1
	s_and_saveexec_b64 s[22:23], vcc
	s_cbranch_execz .LBB1_78
	s_mov_b32 s3, 0xf800000
	v_mul_f32_e32 v8, 0x4f800000, v7
	v_cmp_gt_f32_e32 vcc, s3, v7
	s_nop 1
	v_cndmask_b32_e32 v7, v7, v8, vcc
	v_sqrt_f32_e32 v8, v7
	s_nop 0
	v_add_u32_e32 v9, -1, v8
	v_fma_f32 v10, -v9, v8, v7
	v_cmp_ge_f32_e64 s[18:19], 0, v10
	v_add_u32_e32 v10, 1, v8
	s_nop 0
	v_cndmask_b32_e64 v9, v8, v9, s[18:19]
	v_fma_f32 v8, -v10, v8, v7
	v_cmp_lt_f32_e64 s[18:19], 0, v8
	s_nop 1
	v_cndmask_b32_e64 v8, v9, v10, s[18:19]
	v_mul_f32_e32 v9, 0x37800000, v8
	v_cndmask_b32_e32 v8, v8, v9, vcc
	v_mov_b32_e32 v9, 0x260
	v_cmp_class_f32_e32 vcc, v7, v9
	s_nop 1
	v_cndmask_b32_e32 v7, v8, v7, vcc
	v_div_scale_f32 v8, s[18:19], v7, v7, 1.0
	v_rcp_f32_e32 v9, v8
	s_nop 0
	v_fma_f32 v10, -v8, v9, 1.0
	v_fmac_f32_e32 v9, v10, v9
	v_div_scale_f32 v10, vcc, 1.0, v7, 1.0
	v_mul_f32_e32 v11, v10, v9
	v_fma_f32 v12, -v8, v11, v10
	v_fmac_f32_e32 v11, v12, v9
	v_fma_f32 v8, -v8, v11, v10
	v_div_fmas_f32 v8, v8, v9, v11
	v_div_fixup_f32 v8, v8, v7, 1.0
.LBB1_78:
	s_or_b64 exec, exec, s[22:23]
	v_lshl_add_u64 v[4:5], v[4:5], 2, s[56:57]
	global_store_dword v[4:5], v8, off sc1

.Lcsr_sc_done:
	s_waitcnt lgkmcnt(0)
	s_barrier
	v_and_b32_e32 v4, 7, v88
	v_lshlrev_b32_e32 v4, 6, v4
	v_add_u32_e32 v4, 0x8f20, v4
	ds_read2_b32 v[4:5], v4 offset1:16
	s_waitcnt lgkmcnt(0)
	v_sub_u32_e32 v5, v5, v4
	v_cmp_lt_u32_e32 vcc, 0x400, v5
	s_cmp_eq_u64 vcc, 0
	s_cselect_b32 s34, 1, 0
	s_and_saveexec_b64 s[20:21], s[6:7]
	s_cbranch_execz .Lcsr_rows_done
	v_and_b32_e32 v9, 0x1c0, v3
	ds_read_b32 v9, v9 offset:36640
	v_lshrrev_b32_e32 v10, 4, v0
	v_lshlrev_b32_e32 v10, 10, v10
	s_cmp_eq_u32 s34, 1
	s_cselect_b64 s[24:25], -1, 0
	v_mov_b32_e32 v1, 0x8f20
	v_lshl_add_u32 v1, v0, 2, v1
	ds_read2_b32 v[6:7], v1 offset1:1
	ds_read_b32 v8, v3 offset:38192
	v_lshl_or_b32 v4, s2, 7, v0
	s_mov_b32 s22, 0xc350
	v_cmp_gt_u32_e32 vcc, s22, v4
	s_waitcnt lgkmcnt(0)
	v_add_f32_e32 v1, 1.0, v8
	v_sub_u32_e32 v10, v10, v9
	v_cndmask_b32_e64 v10, 0, v10, s[24:25]
	v_add_u32_e32 v6, v6, v10
	v_add_u32_e32 v7, v7, v10
	s_and_b64 exec, exec, vcc
	s_cbranch_execz .Lcsr_rows_done
	v_mov_b32_e32 v5, 0
	v_lshlrev_b64 v[8:9], 2, v[4:5]
	v_add_u32_e32 v3, v6, v2
	v_lshl_add_u64 v[10:11], s[60:61], 0, v[8:9]
	global_store_dword v[10:11], v3, off sc1
	v_add_u32_e32 v3, v7, v2
	v_lshl_add_u64 v[6:7], s[62:63], 0, v[8:9]
	global_store_dword v[6:7], v3, off sc1
	v_cmp_lt_f32_e32 vcc, 0, v1
	v_mov_b32_e32 v3, v5
	s_and_saveexec_b64 s[22:23], vcc
	s_cbranch_execz .Lcsr_dinv_done
	s_mov_b32 s26, 0xf800000
	v_mul_f32_e32 v3, 0x4f800000, v1
	v_cmp_gt_f32_e32 vcc, s26, v1
	s_nop 1
	v_cndmask_b32_e32 v1, v1, v3, vcc
	v_sqrt_f32_e32 v3, v1
	s_nop 0
	v_add_u32_e32 v6, -1, v3
	v_fma_f32 v7, -v6, v3, v1
	v_cmp_ge_f32_e64 s[24:25], 0, v7
	v_add_u32_e32 v7, 1, v3
	s_nop 0
	v_cndmask_b32_e64 v6, v3, v6, s[24:25]
	v_fma_f32 v3, -v7, v3, v1
	v_cmp_lt_f32_e64 s[24:25], 0, v3
	s_nop 1
	v_cndmask_b32_e64 v3, v6, v7, s[24:25]
	v_mul_f32_e32 v6, 0x37800000, v3
	v_cndmask_b32_e32 v3, v3, v6, vcc
	v_mov_b32_e32 v6, 0x260
	v_cmp_class_f32_e32 vcc, v1, v6
	s_nop 1
	v_cndmask_b32_e32 v1, v3, v1, vcc
	v_div_scale_f32 v3, s[24:25], v1, v1, 1.0
	v_rcp_f32_e32 v6, v3
	s_nop 0
	v_fma_f32 v7, -v3, v6, 1.0
	v_fmac_f32_e32 v6, v7, v6
	v_div_scale_f32 v7, vcc, 1.0, v1, 1.0
	v_mul_f32_e32 v8, v7, v6
	v_fma_f32 v9, -v3, v8, v7
	v_fmac_f32_e32 v8, v9, v6
	v_fma_f32 v3, -v3, v8, v7
	v_div_fmas_f32 v3, v3, v6, v8
	v_div_fixup_f32 v3, v3, v1, 1.0
.Lcsr_dinv_done:
	s_or_b64 exec, exec, s[22:23]
	v_lshl_add_u64 v[4:5], v[4:5], 2, s[56:57]
	global_store_dword v[4:5], v3, off sc1
